# fragment-order gate-logit layout also in the non-256-grid in-proj path (all paths consistent)
# baseline (speedup 1.0000x reference)
.LBB0_196:
	s_ashr_i32 s33, s7, 31
	v_readlane_b32 s57, v253, 35
	s_add_u32 s57, s57, s7
	v_readlane_b32 s59, v253, 37
	s_addc_u32 s33, s59, s33
	v_readlane_b32 s59, v253, 39
	s_add_u32 s59, s59, s7
	v_readlane_b32 s66, v253, 41
	s_addc_u32 s66, s66, 0
	s_add_u32 s59, s59, 0xfffffc00
	s_addc_u32 s66, s66, -1
	v_pk_mul_f32 v[10:11], v[158:159], s[12:13] op_sel_hi:[1,0]
	s_cmp_lt_i32 s0, 4
	v_med3_f32 v16, v10, s52, v179
	v_med3_f32 v11, v11, s52, v179
	v_mov_b32_e32 v10, 0
	s_cselect_b32 s67, s33, s66
	s_cselect_b32 s66, s57, s59
	v_cvt_pk_fp8_f32 v10, v16, v11
	v_lshl_add_u64 v[6:7], s[66:67], 0, v[4:5]
	v_lshlrev_b64 v[8:9], 10, v[2:3]
	v_lshl_add_u64 v[6:7], v[6:7], 0, v[8:9]
	v_lshrrev_b32_e32 v214, 6, v0
	v_lshlrev_b32_e32 v214, 13, v214
	v_and_b32_e32 v215, 63, v0
	v_lshl_add_u32 v214, v215, 3, v214
	v_lshrrev_b32_e32 v215, 8, v2
	v_lshl_add_u32 v214, v215, 18, v214
	s_sub_i32 s32, s7, 0x400
	s_cmp_lt_i32 s0, 4
	s_cselect_b32 s32, s7, s32
	s_mulk_i32 s32, 0xff
	v_add_u32_e32 v214, s32, v214
	v_mov_b32_e32 v215, 0
	v_lshl_add_u64 v[220:221], s[66:67], 0, v[214:215]
	v_add_co_u32_e32 v222, vcc, 0x1000, v220
	s_nop 1
	v_addc_co_u32_e32 v223, vcc, 0, v221, vcc
	v_pk_mul_f32 v[8:9], v[160:161], s[12:13] op_sel_hi:[1,0]
	v_pk_mul_f32 v[14:15], v[154:155], s[12:13] op_sel_hi:[1,0]
	v_med3_f32 v8, v8, s52, v179
	v_med3_f32 v9, v9, s52, v179
	v_cvt_pk_fp8_f32 v10, v8, v9 op_sel:[0,0,1]
	v_med3_f32 v8, v14, s52, v179
	v_med3_f32 v9, v15, s52, v179
	v_mov_b32_e32 v11, 0
	v_cvt_pk_fp8_f32 v11, v8, v9
	v_pk_mul_f32 v[12:13], v[156:157], s[12:13] op_sel_hi:[1,0]
	v_pk_mul_f32 v[14:15], v[142:143], s[12:13] op_sel_hi:[1,0]
	v_med3_f32 v8, v12, s52, v179
	v_med3_f32 v9, v13, s52, v179
	v_cvt_pk_fp8_f32 v11, v8, v9 op_sel:[0,0,1]
	v_pk_mul_f32 v[8:9], v[152:153], s[12:13] op_sel_hi:[1,0]
	v_pk_mul_f32 v[12:13], v[144:145], s[12:13] op_sel_hi:[1,0]
	v_med3_f32 v8, v8, s52, v179
	global_store_dwordx2 v[220:221], v[10:11], off
	v_pk_mul_f32 v[10:11], v[150:151], s[12:13] op_sel_hi:[1,0]
	v_med3_f32 v9, v9, s52, v179
	v_med3_f32 v16, v10, s52, v179
	v_med3_f32 v11, v11, s52, v179
	v_mov_b32_e32 v10, 0
	v_cvt_pk_fp8_f32 v10, v16, v11
	v_mov_b32_e32 v11, 0
	v_pk_mul_f32 v[16:17], v[138:139], s[12:13] op_sel_hi:[1,0]
	s_movk_i32 s0, 0x4000
	v_cvt_pk_fp8_f32 v10, v8, v9 op_sel:[0,0,1]
	v_med3_f32 v8, v14, s52, v179
	v_med3_f32 v9, v15, s52, v179
	v_cvt_pk_fp8_f32 v11, v8, v9
	v_med3_f32 v8, v12, s52, v179
	v_med3_f32 v9, v13, s52, v179
	v_pk_mul_f32 v[12:13], v[146:147], s[12:13] op_sel_hi:[1,0]
	v_cvt_pk_fp8_f32 v11, v8, v9 op_sel:[0,0,1]
	v_med3_f32 v18, v12, s52, v179
	v_med3_f32 v13, v13, s52, v179
	v_mov_b32_e32 v12, 0
	v_cvt_pk_fp8_f32 v12, v18, v13
	global_store_dwordx2 v[220:221], v[10:11], off offset:512
	v_pk_mul_f32 v[10:11], v[148:149], s[12:13] op_sel_hi:[1,0]
	v_mov_b32_e32 v13, 0
	v_med3_f32 v10, v10, s52, v179
	v_med3_f32 v11, v11, s52, v179
	v_cvt_pk_fp8_f32 v12, v10, v11 op_sel:[0,0,1]
	v_med3_f32 v10, v16, s52, v179
	v_med3_f32 v11, v17, s52, v179
	v_cvt_pk_fp8_f32 v13, v10, v11
	v_pk_mul_f32 v[14:15], v[140:141], s[12:13] op_sel_hi:[1,0]
	v_pk_mul_f32 v[16:17], v[126:127], s[12:13] op_sel_hi:[1,0]
	v_med3_f32 v10, v14, s52, v179
	v_med3_f32 v11, v15, s52, v179
	v_cvt_pk_fp8_f32 v13, v10, v11 op_sel:[0,0,1]
	v_add_co_u32_e32 v10, vcc, s0, v6
	v_pk_mul_f32 v[14:15], v[128:129], s[12:13] op_sel_hi:[1,0]
	s_nop 0
	v_addc_co_u32_e32 v11, vcc, 0, v7, vcc
	global_store_dwordx2 v[220:221], v[12:13], off offset:1024
	v_pk_mul_f32 v[12:13], v[134:135], s[12:13] op_sel_hi:[1,0]
	v_pk_mul_f32 v[10:11], v[136:137], s[12:13] op_sel_hi:[1,0]
	v_med3_f32 v18, v12, s52, v179
	v_med3_f32 v13, v13, s52, v179
	v_mov_b32_e32 v12, 0
	v_cvt_pk_fp8_f32 v12, v18, v13
	v_med3_f32 v10, v10, s52, v179
	v_med3_f32 v11, v11, s52, v179
	v_mov_b32_e32 v13, 0
	v_cvt_pk_fp8_f32 v12, v10, v11 op_sel:[0,0,1]
	v_med3_f32 v10, v16, s52, v179
	v_med3_f32 v11, v17, s52, v179
	v_cvt_pk_fp8_f32 v13, v10, v11
	v_med3_f32 v10, v14, s52, v179
	v_med3_f32 v11, v15, s52, v179
	v_lshl_add_u64 v[8:9], v[6:7], 0, s[14:15]
	v_cvt_pk_fp8_f32 v13, v10, v11 op_sel:[0,0,1]
	v_pk_mul_f32 v[10:11], v[132:133], s[12:13] op_sel_hi:[1,0]
	v_pk_mul_f32 v[16:17], v[122:123], s[12:13] op_sel_hi:[1,0]
	v_med3_f32 v10, v10, s52, v179
	global_store_dwordx2 v[220:221], v[12:13], off offset:1536
	v_pk_mul_f32 v[12:13], v[130:131], s[12:13] op_sel_hi:[1,0]
	v_med3_f32 v11, v11, s52, v179
	v_med3_f32 v18, v12, s52, v179
	v_med3_f32 v13, v13, s52, v179
	v_mov_b32_e32 v12, 0
	v_cvt_pk_fp8_f32 v12, v18, v13
	v_mov_b32_e32 v13, 0
	v_pk_mul_f32 v[14:15], v[124:125], s[12:13] op_sel_hi:[1,0]
	s_mov_b32 s0, 0x8000
	v_cvt_pk_fp8_f32 v12, v10, v11 op_sel:[0,0,1]
	v_med3_f32 v10, v16, s52, v179
	v_med3_f32 v11, v17, s52, v179
	v_cvt_pk_fp8_f32 v13, v10, v11
	v_med3_f32 v10, v14, s52, v179
	v_med3_f32 v11, v15, s52, v179
	v_pk_mul_f32 v[16:17], v[110:111], s[12:13] op_sel_hi:[1,0]
	v_cvt_pk_fp8_f32 v13, v10, v11 op_sel:[0,0,1]
	v_add_co_u32_e32 v10, vcc, s0, v6
	v_pk_mul_f32 v[14:15], v[112:113], s[12:13] op_sel_hi:[1,0]
	s_nop 0
	v_addc_co_u32_e32 v11, vcc, 0, v7, vcc
	global_store_dwordx2 v[220:221], v[12:13], off offset:2048
	v_pk_mul_f32 v[12:13], v[118:119], s[12:13] op_sel_hi:[1,0]
	v_pk_mul_f32 v[10:11], v[120:121], s[12:13] op_sel_hi:[1,0]
	v_med3_f32 v18, v12, s52, v179
	v_med3_f32 v13, v13, s52, v179
	v_mov_b32_e32 v12, 0
	v_cvt_pk_fp8_f32 v12, v18, v13
	v_med3_f32 v10, v10, s52, v179
	v_med3_f32 v11, v11, s52, v179
	v_mov_b32_e32 v13, 0
	v_cvt_pk_fp8_f32 v12, v10, v11 op_sel:[0,0,1]
	v_med3_f32 v10, v16, s52, v179
	v_med3_f32 v11, v17, s52, v179
	v_cvt_pk_fp8_f32 v13, v10, v11
	v_med3_f32 v10, v14, s52, v179
	v_med3_f32 v11, v15, s52, v179
	v_lshl_add_u64 v[8:9], v[6:7], 0, s[16:17]
	v_cvt_pk_fp8_f32 v13, v10, v11 op_sel:[0,0,1]
	v_pk_mul_f32 v[10:11], v[116:117], s[12:13] op_sel_hi:[1,0]
	v_pk_mul_f32 v[16:17], v[106:107], s[12:13] op_sel_hi:[1,0]
	v_med3_f32 v10, v10, s52, v179
	global_store_dwordx2 v[220:221], v[12:13], off offset:2560
	v_pk_mul_f32 v[12:13], v[114:115], s[12:13] op_sel_hi:[1,0]
	v_med3_f32 v11, v11, s52, v179
	v_med3_f32 v18, v12, s52, v179
	v_med3_f32 v13, v13, s52, v179
	v_mov_b32_e32 v12, 0
	v_cvt_pk_fp8_f32 v12, v18, v13
	v_mov_b32_e32 v13, 0
	v_pk_mul_f32 v[14:15], v[108:109], s[12:13] op_sel_hi:[1,0]
	v_lshl_add_u64 v[8:9], v[6:7], 0, s[18:19]
	v_cvt_pk_fp8_f32 v12, v10, v11 op_sel:[0,0,1]
	v_med3_f32 v10, v16, s52, v179
	v_med3_f32 v11, v17, s52, v179
	v_cvt_pk_fp8_f32 v13, v10, v11
	v_med3_f32 v10, v14, s52, v179
	v_med3_f32 v11, v15, s52, v179
	v_pk_mul_f32 v[16:17], v[98:99], s[12:13] op_sel_hi:[1,0]
	v_cvt_pk_fp8_f32 v13, v10, v11 op_sel:[0,0,1]
	v_add_co_u32_e32 v10, vcc, s91, v6
	v_pk_mul_f32 v[14:15], v[100:101], s[12:13] op_sel_hi:[1,0]
	s_nop 0
	v_addc_co_u32_e32 v11, vcc, 0, v7, vcc
	global_store_dwordx2 v[220:221], v[12:13], off offset:3072
	v_pk_mul_f32 v[12:13], v[102:103], s[12:13] op_sel_hi:[1,0]
	v_pk_mul_f32 v[10:11], v[104:105], s[12:13] op_sel_hi:[1,0]
	v_med3_f32 v18, v12, s52, v179
	v_med3_f32 v13, v13, s52, v179
	v_mov_b32_e32 v12, 0
	v_cvt_pk_fp8_f32 v12, v18, v13
	v_med3_f32 v10, v10, s52, v179
	v_med3_f32 v11, v11, s52, v179
	v_mov_b32_e32 v13, 0
	v_cvt_pk_fp8_f32 v12, v10, v11 op_sel:[0,0,1]
	v_med3_f32 v10, v16, s52, v179
	v_med3_f32 v11, v17, s52, v179
	v_cvt_pk_fp8_f32 v13, v10, v11
	v_med3_f32 v10, v14, s52, v179
	v_med3_f32 v11, v15, s52, v179
	v_pk_mul_f32 v[16:17], v[90:91], s[12:13] op_sel_hi:[1,0]
	v_cvt_pk_fp8_f32 v13, v10, v11 op_sel:[0,0,1]
	v_pk_mul_f32 v[10:11], v[96:97], s[12:13] op_sel_hi:[1,0]
	v_pk_mul_f32 v[14:15], v[92:93], s[12:13] op_sel_hi:[1,0]
	v_med3_f32 v10, v10, s52, v179
	global_store_dwordx2 v[220:221], v[12:13], off offset:3584
	v_pk_mul_f32 v[12:13], v[94:95], s[12:13] op_sel_hi:[1,0]
	v_med3_f32 v11, v11, s52, v179
	v_med3_f32 v18, v12, s52, v179
	v_med3_f32 v13, v13, s52, v179
	v_mov_b32_e32 v12, 0
	v_cvt_pk_fp8_f32 v12, v18, v13
	v_mov_b32_e32 v13, 0
	s_mov_b64 s[66:67], 0x20000
	v_lshl_add_u64 v[8:9], v[6:7], 0, s[66:67]
	v_cvt_pk_fp8_f32 v12, v10, v11 op_sel:[0,0,1]
	v_med3_f32 v10, v16, s52, v179
	v_med3_f32 v11, v17, s52, v179
	v_cvt_pk_fp8_f32 v13, v10, v11
	v_med3_f32 v10, v14, s52, v179
	v_med3_f32 v11, v15, s52, v179
	v_pk_mul_f32 v[16:17], v[78:79], s[12:13] op_sel_hi:[1,0]
	v_cvt_pk_fp8_f32 v13, v10, v11 op_sel:[0,0,1]
	v_add_co_u32_e32 v10, vcc, s53, v6
	v_pk_mul_f32 v[14:15], v[80:81], s[12:13] op_sel_hi:[1,0]
	s_nop 0
	v_addc_co_u32_e32 v11, vcc, 0, v7, vcc
	global_store_dwordx2 v[222:223], v[12:13], off
	v_pk_mul_f32 v[12:13], v[86:87], s[12:13] op_sel_hi:[1,0]
	v_pk_mul_f32 v[10:11], v[88:89], s[12:13] op_sel_hi:[1,0]
	v_med3_f32 v18, v12, s52, v179
	v_med3_f32 v13, v13, s52, v179
	v_mov_b32_e32 v12, 0
	v_cvt_pk_fp8_f32 v12, v18, v13
	v_med3_f32 v10, v10, s52, v179
	v_med3_f32 v11, v11, s52, v179
	v_mov_b32_e32 v13, 0
	v_cvt_pk_fp8_f32 v12, v10, v11 op_sel:[0,0,1]
	v_med3_f32 v10, v16, s52, v179
	v_med3_f32 v11, v17, s52, v179
	v_cvt_pk_fp8_f32 v13, v10, v11
	v_med3_f32 v10, v14, s52, v179
	v_med3_f32 v11, v15, s52, v179
	v_pk_mul_f32 v[16:17], v[74:75], s[12:13] op_sel_hi:[1,0]
	v_cvt_pk_fp8_f32 v13, v10, v11 op_sel:[0,0,1]
	v_pk_mul_f32 v[10:11], v[84:85], s[12:13] op_sel_hi:[1,0]
	v_pk_mul_f32 v[14:15], v[76:77], s[12:13] op_sel_hi:[1,0]
	v_med3_f32 v10, v10, s52, v179
	global_store_dwordx2 v[222:223], v[12:13], off offset:512
	v_pk_mul_f32 v[12:13], v[82:83], s[12:13] op_sel_hi:[1,0]
	v_med3_f32 v11, v11, s52, v179
	v_med3_f32 v18, v12, s52, v179
	v_med3_f32 v13, v13, s52, v179
	v_mov_b32_e32 v12, 0
	v_cvt_pk_fp8_f32 v12, v18, v13
	v_mov_b32_e32 v13, 0
	v_lshl_add_u64 v[8:9], v[6:7], 0, s[20:21]
	v_cvt_pk_fp8_f32 v12, v10, v11 op_sel:[0,0,1]
	v_med3_f32 v10, v16, s52, v179
	v_med3_f32 v11, v17, s52, v179
	v_cvt_pk_fp8_f32 v13, v10, v11
	v_med3_f32 v10, v14, s52, v179
	v_med3_f32 v11, v15, s52, v179
	v_pk_mul_f32 v[16:17], v[62:63], s[12:13] op_sel_hi:[1,0]
	v_cvt_pk_fp8_f32 v13, v10, v11 op_sel:[0,0,1]
	v_add_co_u32_e32 v10, vcc, s64, v6
	v_pk_mul_f32 v[14:15], v[64:65], s[12:13] op_sel_hi:[1,0]
	s_nop 0
	v_addc_co_u32_e32 v11, vcc, 0, v7, vcc
	global_store_dwordx2 v[222:223], v[12:13], off offset:1024
	v_pk_mul_f32 v[12:13], v[70:71], s[12:13] op_sel_hi:[1,0]
	v_pk_mul_f32 v[10:11], v[72:73], s[12:13] op_sel_hi:[1,0]
	v_med3_f32 v18, v12, s52, v179
	v_med3_f32 v13, v13, s52, v179
	v_mov_b32_e32 v12, 0
	v_cvt_pk_fp8_f32 v12, v18, v13
	v_med3_f32 v10, v10, s52, v179
	v_med3_f32 v11, v11, s52, v179
	v_mov_b32_e32 v13, 0
	v_cvt_pk_fp8_f32 v12, v10, v11 op_sel:[0,0,1]
	v_med3_f32 v10, v16, s52, v179
	v_med3_f32 v11, v17, s52, v179
	v_cvt_pk_fp8_f32 v13, v10, v11
	v_med3_f32 v10, v14, s52, v179
	v_med3_f32 v11, v15, s52, v179
	v_pk_mul_f32 v[16:17], v[58:59], s[12:13] op_sel_hi:[1,0]
	v_cvt_pk_fp8_f32 v13, v10, v11 op_sel:[0,0,1]
	v_pk_mul_f32 v[10:11], v[68:69], s[12:13] op_sel_hi:[1,0]
	v_pk_mul_f32 v[14:15], v[60:61], s[12:13] op_sel_hi:[1,0]
	v_med3_f32 v10, v10, s52, v179
	global_store_dwordx2 v[222:223], v[12:13], off offset:1536
	v_pk_mul_f32 v[12:13], v[66:67], s[12:13] op_sel_hi:[1,0]
	v_med3_f32 v11, v11, s52, v179
	v_med3_f32 v18, v12, s52, v179
	v_med3_f32 v13, v13, s52, v179
	v_mov_b32_e32 v12, 0
	v_cvt_pk_fp8_f32 v12, v18, v13
	v_mov_b32_e32 v13, 0
	v_lshl_add_u64 v[8:9], v[6:7], 0, s[22:23]
	v_cvt_pk_fp8_f32 v12, v10, v11 op_sel:[0,0,1]
	v_med3_f32 v10, v16, s52, v179
	v_med3_f32 v11, v17, s52, v179
	v_cvt_pk_fp8_f32 v13, v10, v11
	v_med3_f32 v10, v14, s52, v179
	v_med3_f32 v11, v15, s52, v179
	v_pk_mul_f32 v[16:17], v[46:47], s[12:13] op_sel_hi:[1,0]
	v_cvt_pk_fp8_f32 v13, v10, v11 op_sel:[0,0,1]
	v_add_co_u32_e32 v10, vcc, s65, v6
	v_pk_mul_f32 v[14:15], v[48:49], s[12:13] op_sel_hi:[1,0]
	s_nop 0
	v_addc_co_u32_e32 v11, vcc, 0, v7, vcc
	global_store_dwordx2 v[222:223], v[12:13], off offset:2048
	v_pk_mul_f32 v[12:13], v[54:55], s[12:13] op_sel_hi:[1,0]
	v_pk_mul_f32 v[10:11], v[56:57], s[12:13] op_sel_hi:[1,0]
	v_med3_f32 v18, v12, s52, v179
	v_med3_f32 v13, v13, s52, v179
	v_mov_b32_e32 v12, 0
	v_cvt_pk_fp8_f32 v12, v18, v13
	v_med3_f32 v10, v10, s52, v179
	v_med3_f32 v11, v11, s52, v179
	v_mov_b32_e32 v13, 0
	v_cvt_pk_fp8_f32 v12, v10, v11 op_sel:[0,0,1]
	v_med3_f32 v10, v16, s52, v179
	v_med3_f32 v11, v17, s52, v179
	v_cvt_pk_fp8_f32 v13, v10, v11
	v_med3_f32 v10, v14, s52, v179
	v_med3_f32 v11, v15, s52, v179
	v_pk_mul_f32 v[16:17], v[42:43], s[12:13] op_sel_hi:[1,0]
	v_cvt_pk_fp8_f32 v13, v10, v11 op_sel:[0,0,1]
	v_pk_mul_f32 v[10:11], v[52:53], s[12:13] op_sel_hi:[1,0]
	v_pk_mul_f32 v[14:15], v[44:45], s[12:13] op_sel_hi:[1,0]
	v_med3_f32 v10, v10, s52, v179
	global_store_dwordx2 v[222:223], v[12:13], off offset:2560
	v_pk_mul_f32 v[12:13], v[50:51], s[12:13] op_sel_hi:[1,0]
	v_med3_f32 v11, v11, s52, v179
	v_med3_f32 v18, v12, s52, v179
	v_med3_f32 v13, v13, s52, v179
	v_mov_b32_e32 v12, 0
	v_cvt_pk_fp8_f32 v12, v18, v13
	v_mov_b32_e32 v13, 0
	v_lshl_add_u64 v[8:9], v[6:7], 0, s[40:41]
	v_add_co_u32_e32 v6, vcc, s31, v6
	v_cvt_pk_fp8_f32 v12, v10, v11 op_sel:[0,0,1]
	v_med3_f32 v10, v16, s52, v179
	v_med3_f32 v11, v17, s52, v179
	v_cvt_pk_fp8_f32 v13, v10, v11
	v_med3_f32 v10, v14, s52, v179
	v_med3_f32 v11, v15, s52, v179
	v_addc_co_u32_e32 v7, vcc, 0, v7, vcc
	v_cvt_pk_fp8_f32 v13, v10, v11 op_sel:[0,0,1]
	v_pk_mul_f32 v[10:11], v[38:39], s[12:13] op_sel_hi:[1,0]
	v_pk_mul_f32 v[14:15], v[34:35], s[12:13] op_sel_hi:[1,0]
	v_med3_f32 v16, v10, s52, v179
	v_med3_f32 v11, v11, s52, v179
	v_mov_b32_e32 v10, 0
	v_cvt_pk_fp8_f32 v10, v16, v11
	global_store_dwordx2 v[222:223], v[12:13], off offset:3072
	v_pk_mul_f32 v[6:7], v[40:41], s[12:13] op_sel_hi:[1,0]
	v_mov_b32_e32 v11, 0
	v_med3_f32 v6, v6, s52, v179
	v_med3_f32 v7, v7, s52, v179
	v_cvt_pk_fp8_f32 v10, v6, v7 op_sel:[0,0,1]
	v_med3_f32 v6, v14, s52, v179
	v_med3_f32 v7, v15, s52, v179
	v_cvt_pk_fp8_f32 v11, v6, v7
	v_pk_mul_f32 v[12:13], v[36:37], s[12:13] op_sel_hi:[1,0]
	s_nop 0
	v_med3_f32 v6, v12, s52, v179
	v_med3_f32 v7, v13, s52, v179
	v_cvt_pk_fp8_f32 v11, v6, v7 op_sel:[0,0,1]
	global_store_dwordx2 v[222:223], v[10:11], off offset:3584
	s_cbranch_execnz .LBB0_195
